# P12 epilogue: the eight expert-weight loads issued together with counted waits, plus earlier edits
# speedup vs baseline: 1.0344x; 1.0013x over previous
.LBB0_1283:
	v_add_u32_e32 v148, s40, v152
	v_ashrrev_i32_e32 v149, 31, v148
	v_lshl_add_u64 v[150:151], v[148:149], 2, s[12:13]
	global_load_dword v164, v[150:151], off
	global_load_dword v166, v[150:151], off offset:64
	global_load_dword v168, v[150:151], off offset:128
	global_load_dword v170, v[150:151], off offset:192
	global_load_dword v172, v[150:151], off offset:512
	global_load_dword v174, v[150:151], off offset:576
	global_load_dword v176, v[150:151], off offset:640
	global_load_dword v178, v[150:151], off offset:704
	v_lshl_or_b32 v162, s79, 8, v153
	v_lshlrev_b64 v[148:149], 12, v[148:149]
	v_ashrrev_i32_e32 v163, 31, v162
	v_lshl_add_u64 v[148:149], s[10:11], 0, v[148:149]
	v_lshl_add_u64 v[148:149], v[162:163], 1, v[148:149]
	s_waitcnt vmcnt(7)
	v_pk_mul_f32 v[126:127], v[126:127], v[164:165] op_sel_hi:[1,0]
	v_pk_mul_f32 v[124:125], v[124:125], v[164:165] op_sel_hi:[1,0]
	v_pk_mul_f32 v[122:123], v[122:123], v[164:165] op_sel_hi:[1,0]
	v_pk_mul_f32 v[120:121], v[120:121], v[164:165] op_sel_hi:[1,0]
	v_pk_mul_f32 v[118:119], v[118:119], v[164:165] op_sel_hi:[1,0]
	v_pk_mul_f32 v[116:117], v[116:117], v[164:165] op_sel_hi:[1,0]
	v_pk_mul_f32 v[162:163], v[114:115], v[164:165] op_sel_hi:[1,0]
	v_pk_mul_f32 v[160:161], v[112:113], v[164:165] op_sel_hi:[1,0]
	v_cvt_pk_bf16_f32 v112, v124, v125
	v_cvt_pk_bf16_f32 v113, v126, v127
	v_cvt_pk_bf16_f32 v114, v120, v121
	v_cvt_pk_bf16_f32 v115, v122, v123
	v_cvt_pk_bf16_f32 v116, v116, v117
	v_cvt_pk_bf16_f32 v117, v118, v119
	v_cvt_pk_bf16_f32 v118, v160, v161
	v_cvt_pk_bf16_f32 v119, v162, v163
	global_store_dwordx4 v[148:149], v[112:115], off
	global_store_dwordx4 v[148:149], v[116:119], off offset:256
	s_nop 1
	v_lshl_add_u64 v[114:115], v[148:149], 0, s[18:19]
	v_add_co_u32_e32 v116, vcc, s59, v148
	s_waitcnt vmcnt(8)
	v_pk_mul_f32 v[110:111], v[110:111], v[166:167] op_sel_hi:[1,0]
	v_pk_mul_f32 v[108:109], v[108:109], v[166:167] op_sel_hi:[1,0]
	v_pk_mul_f32 v[106:107], v[106:107], v[166:167] op_sel_hi:[1,0]
	v_pk_mul_f32 v[104:105], v[104:105], v[166:167] op_sel_hi:[1,0]
	v_addc_co_u32_e32 v117, vcc, 0, v149, vcc
	v_pk_mul_f32 v[102:103], v[102:103], v[166:167] op_sel_hi:[1,0]
	v_pk_mul_f32 v[100:101], v[100:101], v[166:167] op_sel_hi:[1,0]
	v_pk_mul_f32 v[118:119], v[98:99], v[166:167] op_sel_hi:[1,0]
	v_pk_mul_f32 v[112:113], v[96:97], v[166:167] op_sel_hi:[1,0]
	v_cvt_pk_bf16_f32 v96, v108, v109
	v_cvt_pk_bf16_f32 v97, v110, v111
	v_cvt_pk_bf16_f32 v98, v104, v105
	v_cvt_pk_bf16_f32 v99, v106, v107
	v_cvt_pk_bf16_f32 v100, v100, v101
	v_cvt_pk_bf16_f32 v101, v102, v103
	v_cvt_pk_bf16_f32 v102, v112, v113
	v_cvt_pk_bf16_f32 v103, v118, v119
	global_store_dwordx4 v[116:117], v[96:99], off
	global_store_dwordx4 v[114:115], v[100:103], off offset:256
	s_nop 1
	v_lshl_add_u64 v[98:99], v[148:149], 0, s[20:21]
	v_add_co_u32_e32 v100, vcc, s71, v148
	s_waitcnt vmcnt(9)
	v_pk_mul_f32 v[94:95], v[94:95], v[168:169] op_sel_hi:[1,0]
	v_pk_mul_f32 v[92:93], v[92:93], v[168:169] op_sel_hi:[1,0]
	v_pk_mul_f32 v[90:91], v[90:91], v[168:169] op_sel_hi:[1,0]
	v_pk_mul_f32 v[88:89], v[88:89], v[168:169] op_sel_hi:[1,0]
	v_addc_co_u32_e32 v101, vcc, 0, v149, vcc
	v_pk_mul_f32 v[86:87], v[86:87], v[168:169] op_sel_hi:[1,0]
	v_pk_mul_f32 v[84:85], v[84:85], v[168:169] op_sel_hi:[1,0]
	v_pk_mul_f32 v[102:103], v[82:83], v[168:169] op_sel_hi:[1,0]
	v_pk_mul_f32 v[96:97], v[80:81], v[168:169] op_sel_hi:[1,0]
	v_cvt_pk_bf16_f32 v80, v92, v93
	v_cvt_pk_bf16_f32 v81, v94, v95
	v_cvt_pk_bf16_f32 v82, v88, v89
	v_cvt_pk_bf16_f32 v83, v90, v91
	v_cvt_pk_bf16_f32 v84, v84, v85
	v_cvt_pk_bf16_f32 v85, v86, v87
	v_cvt_pk_bf16_f32 v86, v96, v97
	v_cvt_pk_bf16_f32 v87, v102, v103
	global_store_dwordx4 v[100:101], v[80:83], off
	global_store_dwordx4 v[98:99], v[84:87], off offset:256
	s_nop 1
	v_lshl_add_u64 v[82:83], v[148:149], 0, s[22:23]
	v_add_co_u32_e32 v84, vcc, s72, v148
	s_waitcnt vmcnt(10)
	v_pk_mul_f32 v[78:79], v[78:79], v[170:171] op_sel_hi:[1,0]
	v_pk_mul_f32 v[76:77], v[76:77], v[170:171] op_sel_hi:[1,0]
	v_pk_mul_f32 v[74:75], v[74:75], v[170:171] op_sel_hi:[1,0]
	v_pk_mul_f32 v[72:73], v[72:73], v[170:171] op_sel_hi:[1,0]
	v_addc_co_u32_e32 v85, vcc, 0, v149, vcc
	v_pk_mul_f32 v[62:63], v[62:63], v[170:171] op_sel_hi:[1,0]
	v_pk_mul_f32 v[60:61], v[60:61], v[170:171] op_sel_hi:[1,0]
	v_pk_mul_f32 v[86:87], v[58:59], v[170:171] op_sel_hi:[1,0]
	v_pk_mul_f32 v[80:81], v[56:57], v[170:171] op_sel_hi:[1,0]
	v_cvt_pk_bf16_f32 v56, v76, v77
	v_cvt_pk_bf16_f32 v57, v78, v79
	v_cvt_pk_bf16_f32 v58, v72, v73
	v_cvt_pk_bf16_f32 v59, v74, v75
	v_cvt_pk_bf16_f32 v60, v60, v61
	v_cvt_pk_bf16_f32 v61, v62, v63
	v_cvt_pk_bf16_f32 v62, v80, v81
	v_cvt_pk_bf16_f32 v63, v86, v87
	global_store_dwordx4 v[84:85], v[56:59], off
	global_store_dwordx4 v[82:83], v[60:63], off offset:256
	s_nop 1
	v_lshl_add_u64 v[58:59], v[148:149], 0, s[24:25]
	v_add_co_u32_e32 v60, vcc, s73, v148
	s_waitcnt vmcnt(11)
	v_pk_mul_f32 v[46:47], v[46:47], v[172:173] op_sel_hi:[1,0]
	v_pk_mul_f32 v[44:45], v[44:45], v[172:173] op_sel_hi:[1,0]
	v_pk_mul_f32 v[62:63], v[42:43], v[172:173] op_sel_hi:[1,0]
	v_pk_mul_f32 v[42:43], v[40:41], v[172:173] op_sel_hi:[1,0]
	v_addc_co_u32_e32 v61, vcc, 0, v149, vcc
	v_pk_mul_f32 v[66:67], v[66:67], v[172:173] op_sel_hi:[1,0]
	v_pk_mul_f32 v[64:65], v[64:65], v[172:173] op_sel_hi:[1,0]
	v_pk_mul_f32 v[70:71], v[70:71], v[172:173] op_sel_hi:[1,0]
	v_pk_mul_f32 v[56:57], v[68:69], v[172:173] op_sel_hi:[1,0]
	v_cvt_pk_bf16_f32 v40, v44, v45
	v_cvt_pk_bf16_f32 v41, v46, v47
	v_cvt_pk_bf16_f32 v42, v42, v43
	v_cvt_pk_bf16_f32 v43, v62, v63
	v_cvt_pk_bf16_f32 v44, v64, v65
	v_cvt_pk_bf16_f32 v45, v66, v67
	v_cvt_pk_bf16_f32 v46, v56, v57
	v_cvt_pk_bf16_f32 v47, v70, v71
	global_store_dwordx4 v[60:61], v[40:43], off
	global_store_dwordx4 v[58:59], v[44:47], off offset:256
	s_nop 1
	v_lshl_add_u64 v[42:43], v[148:149], 0, s[26:27]
	v_add_co_u32_e32 v44, vcc, s74, v148
	s_waitcnt vmcnt(12)
	v_pk_mul_f32 v[30:31], v[30:31], v[174:175] op_sel_hi:[1,0]
	v_pk_mul_f32 v[28:29], v[28:29], v[174:175] op_sel_hi:[1,0]
	v_pk_mul_f32 v[46:47], v[26:27], v[174:175] op_sel_hi:[1,0]
	v_pk_mul_f32 v[26:27], v[24:25], v[174:175] op_sel_hi:[1,0]
	v_addc_co_u32_e32 v45, vcc, 0, v149, vcc
	v_pk_mul_f32 v[50:51], v[50:51], v[174:175] op_sel_hi:[1,0]
	v_pk_mul_f32 v[48:49], v[48:49], v[174:175] op_sel_hi:[1,0]
	v_pk_mul_f32 v[54:55], v[54:55], v[174:175] op_sel_hi:[1,0]
	v_pk_mul_f32 v[40:41], v[52:53], v[174:175] op_sel_hi:[1,0]
	v_cvt_pk_bf16_f32 v24, v28, v29
	v_cvt_pk_bf16_f32 v25, v30, v31
	v_cvt_pk_bf16_f32 v26, v26, v27
	v_cvt_pk_bf16_f32 v27, v46, v47
	v_cvt_pk_bf16_f32 v28, v48, v49
	v_cvt_pk_bf16_f32 v29, v50, v51
	v_cvt_pk_bf16_f32 v30, v40, v41
	v_cvt_pk_bf16_f32 v31, v54, v55
	global_store_dwordx4 v[44:45], v[24:27], off
	global_store_dwordx4 v[42:43], v[28:31], off offset:256
	s_nop 1
	v_lshl_add_u64 v[26:27], v[148:149], 0, s[28:29]
	v_add_co_u32_e32 v28, vcc, s75, v148
	s_waitcnt vmcnt(13)
	v_pk_mul_f32 v[14:15], v[14:15], v[176:177] op_sel_hi:[1,0]
	v_pk_mul_f32 v[12:13], v[12:13], v[176:177] op_sel_hi:[1,0]
	v_pk_mul_f32 v[30:31], v[10:11], v[176:177] op_sel_hi:[1,0]
	v_pk_mul_f32 v[10:11], v[8:9], v[176:177] op_sel_hi:[1,0]
	v_addc_co_u32_e32 v29, vcc, 0, v149, vcc
	v_pk_mul_f32 v[34:35], v[34:35], v[176:177] op_sel_hi:[1,0]
	v_pk_mul_f32 v[32:33], v[32:33], v[176:177] op_sel_hi:[1,0]
	v_pk_mul_f32 v[38:39], v[38:39], v[176:177] op_sel_hi:[1,0]
	v_pk_mul_f32 v[24:25], v[36:37], v[176:177] op_sel_hi:[1,0]
	v_cvt_pk_bf16_f32 v8, v12, v13
	v_cvt_pk_bf16_f32 v9, v14, v15
	v_cvt_pk_bf16_f32 v10, v10, v11
	v_cvt_pk_bf16_f32 v11, v30, v31
	v_cvt_pk_bf16_f32 v12, v32, v33
	v_cvt_pk_bf16_f32 v13, v34, v35
	v_cvt_pk_bf16_f32 v14, v24, v25
	v_cvt_pk_bf16_f32 v15, v38, v39
	global_store_dwordx4 v[28:29], v[8:11], off
	global_store_dwordx4 v[26:27], v[12:15], off offset:256
	s_nop 1
	s_andn2_b64 vcc, exec, s[2:3]
	v_add_co_u32_e64 v12, s[2:3], s76, v148
	v_lshl_add_u64 v[10:11], v[148:149], 0, s[30:31]
	s_nop 0
	v_addc_co_u32_e64 v13, s[2:3], 0, v149, s[2:3]
	s_mov_b64 s[2:3], -1
	s_waitcnt vmcnt(14)
	v_pk_mul_f32 v[6:7], v[6:7], v[178:179] op_sel_hi:[1,0]
	v_pk_mul_f32 v[4:5], v[4:5], v[178:179] op_sel_hi:[1,0]
	v_pk_mul_f32 v[14:15], v[2:3], v[178:179] op_sel_hi:[1,0]
	v_pk_mul_f32 v[2:3], v[0:1], v[178:179] op_sel_hi:[1,0]
	v_pk_mul_f32 v[18:19], v[18:19], v[178:179] op_sel_hi:[1,0]
	v_pk_mul_f32 v[16:17], v[16:17], v[178:179] op_sel_hi:[1,0]
	v_pk_mul_f32 v[22:23], v[22:23], v[178:179] op_sel_hi:[1,0]
	v_pk_mul_f32 v[8:9], v[20:21], v[178:179] op_sel_hi:[1,0]
	v_cvt_pk_bf16_f32 v0, v4, v5
	v_cvt_pk_bf16_f32 v1, v6, v7
	v_cvt_pk_bf16_f32 v2, v2, v3
	v_cvt_pk_bf16_f32 v3, v14, v15
	v_cvt_pk_bf16_f32 v4, v16, v17
	v_cvt_pk_bf16_f32 v5, v18, v19
	v_cvt_pk_bf16_f32 v6, v8, v9
	v_cvt_pk_bf16_f32 v7, v22, v23
	global_store_dwordx4 v[12:13], v[0:3], off
	global_store_dwordx4 v[10:11], v[4:7], off offset:256
	s_cbranch_vccnz .LBB0_1272
	s_andn2_b64 vcc, exec, s[8:9]
	s_cbranch_vccnz .LBB0_1271
	s_barrier
	s_branch .LBB0_1271
